# s17 + PROJ unit order per XCD: last pass = CQK/CV columns for all 8 row tiles (x1 pre-pass finds them in the XCD's L2)
# baseline (speedup 1.0000x reference)
.LBB0_977:
	s_add_i32 s28, s28, 1
	s_mul_i32 s21, s28, s27
	s_mul_hi_u32 s36, s28, s18
	s_add_i32 s36, s36, s21
	s_mul_i32 s21, s28, s18
	v_readlane_b32 s37, v252, 0
	s_add_u32 s42, s21, s37
	v_readlane_b32 s21, v253, 35
	s_addc_u32 s43, s36, s21
	v_mov_b64_e32 v[0:1], 0x600
	v_cmp_lt_i64_e64 s[38:39], s[42:43], v[0:1]
	v_mov_b64_e32 v[0:1], 0x5ff
	v_cmp_gt_i64_e32 vcc, s[42:43], v[0:1]
	s_cbranch_vccnz .LBB0_979
	s_ashr_i32 s20, s42, 31
	s_lshr_b32 s20, s20, 29
	s_add_i32 s20, s42, s20
	s_ashr_i32 s21, s20, 3
	s_lshr_b32 s36, s21, 5
	s_and_b32 s37, s21, 31
	s_cmp_lt_u32 s36, 4
	s_cbranch_scc0 .Lproj_lastpasses
	s_cmp_ge_u32 s36, 2
	s_cselect_b32 s100, 32, 0
	s_add_i32 s21, s21, s100
	s_branch .Lproj_remap_done
.Lproj_lastpasses:
	s_and_b32 s100, s37, 7
	s_lshr_b32 s37, s37, 3
	s_cmp_eq_u32 s36, 4
	s_cselect_b32 s36, 4, 0
	s_add_i32 s37, s37, s36
	s_lshl_b32 s37, s37, 2
	s_and_b32 s36, s100, 3
	s_add_i32 s37, s37, s36
	s_lshr_b32 s100, s100, 2
	s_mul_i32 s100, s100, 0x60
	s_add_i32 s21, s100, s37
	s_add_i32 s21, s21, 64
.Lproj_remap_done:
	s_and_b32 s20, s20, -8
	s_sub_i32 s20, s42, s20
	s_cmp_lt_i32 s20, 0
	s_movk_i32 s36, 0xc1
	s_cselect_b32 s36, s36, 0xc0
	s_mul_i32 s20, s20, s36
	s_add_i32 s20, s20, s21
	s_mul_hi_i32 s21, s20, 0x2aaaaaab
	s_lshr_b32 s36, s21, 31
	s_ashr_i32 s21, s21, 4
	s_add_i32 s21, s21, s36
	s_lshl_b32 s36, s21, 2
	s_sub_i32 s37, 64, s36
	s_min_i32 s37, s37, 4
	s_abs_i32 s40, s37
	v_cvt_f32_u32_e32 v0, s40
	s_sub_i32 s42, 0, s40
	s_mulk_i32 s21, 0x60
	s_sub_i32 s21, s20, s21
	v_rcp_iflag_f32_e32 v0, v0
	s_abs_i32 s20, s21
	s_xor_b32 s41, s21, s37
	s_ashr_i32 s41, s41, 31
	v_mul_f32_e32 v0, 0x4f7ffffe, v0
	v_cvt_u32_f32_e32 v0, v0
	s_nop 0
	v_readfirstlane_b32 s43, v0
	s_mul_i32 s42, s42, s43
	s_mul_hi_u32 s42, s43, s42
	s_add_i32 s43, s43, s42
	s_mul_hi_u32 s42, s20, s43
	s_mul_i32 s43, s42, s40
	s_sub_i32 s20, s20, s43
	s_add_i32 s44, s42, 1
	s_sub_i32 s43, s20, s40
	s_cmp_ge_u32 s20, s40
	s_cselect_b32 s42, s44, s42
	s_cselect_b32 s20, s43, s20
	s_add_i32 s43, s42, 1
	s_cmp_ge_u32 s20, s40
	s_cselect_b32 s20, s43, s42
	s_xor_b32 s20, s20, s41
	s_sub_i32 s20, s20, s41
	s_mul_i32 s37, s20, s37
	s_sub_i32 s21, s21, s37
	s_add_i32 s40, s36, s21
